# v76 + one static s_setprio 1 for waves 4-7 during the attention work-queue phase (strategy 4, timing-only)
# baseline (speedup 1.0000x reference)
.LBB0_3599:
	v_cvt_f32_u32_e32 v0, s48
	s_mov_b32 s0, 0x3fb8aa3b
	s_mov_b32 s4, 0xc2ce8ed0
	s_mov_b32 s5, 0x42b17218
	v_mul_f32_e32 v0, 0xbe99999a, v0
	v_mul_f32_e32 v2, 0x3fb8aa3b, v0
	v_fma_f32 v3, v0, s0, -v2
	v_rndne_f32_e32 v4, v2
	v_fmac_f32_e32 v3, 0x32a5705f, v0
	v_sub_f32_e32 v2, v2, v4
	v_add_f32_e32 v2, v2, v3
	v_cvt_i32_f32_e32 v4, v4
	v_exp_f32_e32 v2, v2
	s_waitcnt lgkmcnt(1)
	v_add_f32_e32 v3, v58, v59
	v_mul_f32_e32 v5, 0x3fb8aa3b, v3
	v_rndne_f32_e32 v6, v5
	v_ldexp_f32 v2, v2, v4
	v_fma_f32 v4, v3, s0, -v5
	v_fmac_f32_e32 v4, 0x32a5705f, v3
	v_sub_f32_e32 v5, v5, v6
	v_add_f32_e32 v4, v5, v4
	v_exp_f32_e32 v4, v4
	v_cvt_i32_f32_e32 v5, v6
	v_cmp_ngt_f32_e32 vcc, s4, v0
	s_lshl_b32 s92, s48, 3
	s_lshl_b32 s63, s48, 8
	v_cndmask_b32_e32 v2, 0, v2, vcc
	v_cmp_nlt_f32_e32 vcc, s5, v0
	v_ldexp_f32 v4, v4, v5
	v_cmp_eq_u32_e64 s[74:75], 0, v147
	v_cndmask_b32_e32 v0, v234, v2, vcc
	v_mov_b32_e32 v2, 0x3f4ccccd
	v_fmamk_f32 v0, v0, 0xbf19999a, v2
	s_waitcnt lgkmcnt(0)
	v_add_f32_e32 v2, v55, v57
	v_cmp_ngt_f32_e32 vcc, s4, v3
	v_mul_f32_e32 v5, 0x3fb8aa3b, v2
	v_fma_f32 v6, v2, s0, -v5
	v_cndmask_b32_e32 v4, 0, v4, vcc
	v_cmp_nlt_f32_e32 vcc, s5, v3
	s_lshl_b32 s0, s48, 19
	v_rndne_f32_e32 v7, v5
	v_cndmask_b32_e32 v3, v234, v4, vcc
	v_cmp_ngt_f32_e32 vcc, s4, v2
	s_lshl_b32 s4, s48, 7
	s_add_u32 s2, s84, s2
	s_addc_u32 s3, s85, s3
	s_add_u32 s50, s2, 0x20000
	s_addc_u32 s51, s3, 0
	s_add_u32 s72, s2, 0x30000
	s_addc_u32 s73, s3, 0
	s_add_u32 s2, s84, 0x22600000
	s_addc_u32 s3, s85, 0
	v_writelane_b32 v254, s2, 60
	v_fmac_f32_e32 v6, 0x32a5705f, v2
	v_sub_f32_e32 v5, v5, v7
	v_writelane_b32 v254, s3, 61
	s_add_u32 s2, s84, 0x23a00000
	v_writelane_b32 v254, s2, 62
	s_addc_u32 s2, s85, 0
	v_writelane_b32 v254, s2, 63
	s_add_u32 s2, s84, 0x23600000
	v_writelane_b32 v255, s2, 0
	s_addc_u32 s2, s85, 0
	v_writelane_b32 v255, s2, 1
	s_add_u32 s2, s84, 0x38400000
	s_addc_u32 s3, s85, 0
	v_writelane_b32 v255, s2, 2
	v_add_f32_e32 v5, v5, v6
	v_exp_f32_e32 v5, v5
	v_writelane_b32 v255, s3, 3
	s_add_u32 s2, s84, 0x29000000
	s_addc_u32 s3, s85, 0
	v_writelane_b32 v255, s2, 4
	v_cvt_i32_f32_e32 v6, v7
	v_sub_f32_e32 v152, 1.0, v0
	v_writelane_b32 v255, s3, 5
	s_add_u32 s2, s84, 0x2a000000
	v_writelane_b32 v255, s2, 6
	s_addc_u32 s2, s85, 0
	v_writelane_b32 v255, s2, 7
	s_add_u32 s2, s84, 0x2b000000
	v_writelane_b32 v255, s2, 8
	s_addc_u32 s2, s85, 0
	v_writelane_b32 v255, s2, 9
	s_add_u32 s2, s84, 0x23e00000
	s_addc_u32 s3, s85, 0
	v_writelane_b32 v255, s2, 10
	v_ldexp_f32 v4, v5, v6
	v_cndmask_b32_e32 v4, 0, v4, vcc
	v_writelane_b32 v255, s3, 11
	s_add_u32 s2, s84, 0x2c000000
	s_addc_u32 s3, s85, 0
	v_writelane_b32 v255, s2, 12
	s_add_u32 s0, s84, s0
	v_cmp_nlt_f32_e32 vcc, s5, v2
	v_writelane_b32 v255, s3, 13
	s_addc_u32 s2, s85, 0
	s_add_u32 s3, s0, 0x2c200000
	v_writelane_b32 v255, s3, 14
	s_addc_u32 s3, s2, 0
	v_writelane_b32 v255, s3, 15
	v_writelane_b32 v255, s0, 16
	s_add_u32 s0, s0, 0x2c300000
	v_writelane_b32 v255, s0, 17
	v_writelane_b32 v255, s2, 18
	s_addc_u32 s0, s2, 0
	v_writelane_b32 v255, s0, 19
	s_add_u32 s0, s84, 0x27800000
	v_writelane_b32 v255, s0, 20
	s_addc_u32 s0, s85, 0
	v_writelane_b32 v255, s0, 21
	s_add_u32 s0, s84, 0x27000000
	v_writelane_b32 v255, s0, 22
	s_addc_u32 s0, s85, 0
	v_writelane_b32 v255, s0, 23
	s_add_u32 s0, s84, 0x28800000
	v_writelane_b32 v255, s0, 24
	s_addc_u32 s0, s85, 0
	v_writelane_b32 v255, s0, 25
	s_add_u32 s0, s84, 0x28000000
	v_writelane_b32 v255, s0, 26
	s_addc_u32 s0, s85, 0
	s_add_u32 s2, s84, 0x15b00000
	v_writelane_b32 v255, s0, 27
	s_addc_u32 s3, s85, 0
	v_writelane_b32 v255, s2, 28
	s_mov_b32 s5, s93
	v_cndmask_b32_e32 v2, v234, v4, vcc
	v_writelane_b32 v255, s3, 29
	s_add_u32 s2, s84, 0x8d00000
	s_addc_u32 s3, s85, 0
	v_writelane_b32 v255, s2, 30
	s_add_u32 s0, s84, 0x8900100
	v_sub_f32_e32 v2, v3, v2
	v_writelane_b32 v255, s3, 31
	s_mov_b64 s[2:3], 0
	v_writelane_b32 v255, s0, 32
	s_addc_u32 s0, s85, 0
	v_writelane_b32 v254, s2, 55
	v_writelane_b32 v255, s0, 33
	v_add_f32_e32 v148, v0, v2
	v_writelane_b32 v254, s3, 56
	s_lshl_b64 s[2:3], s[92:93], 2
	v_writelane_b32 v255, s2, 34
	v_mov_b32_e32 v149, v148
	s_mov_b32 s56, 0x38400000
	v_writelane_b32 v255, s3, 35
	s_lshl_b64 s[2:3], s[4:5], 2
	v_writelane_b32 v255, s2, 36
	s_movk_i32 s57, 0x80
	s_movk_i32 s58, 0x84
	v_writelane_b32 v255, s3, 37
	v_writelane_b32 v255, s50, 38
	v_readlane_b32 s59, v254, 27
	s_movk_i32 s60, 0x7f
	v_writelane_b32 v255, s51, 39
	v_writelane_b32 v255, s72, 40
	s_mov_b32 s61, 0xff800000
	s_nop 0
	v_writelane_b32 v255, s73, 41
	v_writelane_b32 v255, s74, 42
	s_nop 1
	v_writelane_b32 v255, s75, 43
	v_writelane_b32 v255, s63, 44
	v_writelane_b32 v255, s84, 45
	s_nop 1
	v_writelane_b32 v255, s85, 46
	s_mov_b32 s32, 0
	v_readlane_b32 s98, v254, 6
	s_nop 3
	s_cmp_ge_u32 s98, 4
	s_cbranch_scc0 .Lprio_skip
	s_setprio 1
.Lprio_skip:
	s_branch .LBB0_3603
.LBB0_3600:
	s_or_b64 exec, exec, s[4:5]
	v_readlane_b32 s4, v254, 55
	v_readlane_b32 s5, v254, 56

.LBB0_3786:
	s_setprio 0
	v_readlane_b32 s74, v254, 33
	v_readlane_b32 s80, v254, 35
	v_readlane_b32 s84, v254, 37
	v_readlane_b32 s86, v254, 39
	v_readlane_b32 s90, v254, 41
	v_readlane_b32 s75, v254, 34
	v_readlane_b32 s81, v254, 36
	v_readlane_b32 s85, v254, 38
	v_readlane_b32 s87, v254, 40
	v_readlane_b32 s91, v254, 42
	s_mov_b32 s59, 0x41000000
	s_mov_b64 s[60:61], 0x400
	v_readlane_b32 s4, v254, 57
